# attention main-loop head padded to a 64-byte boundary (was at offset 4 mod 8); otherwise v38
# speedup vs baseline: 1.0032x; 1.0032x over previous
; __device__ __forceinline__ int v_rd_base(int lane) { return ((lane & 3) << 3) | (((lane >> 2) & 3) << 6) | (((lane >> 4) & 1) << 5) | (((lane >> 5) & 1) << 8); }
; #define ATT_WAIT_BAR() asm volatile("s_waitcnt vmcnt(0) lgkmcnt(0)\n\ts_barrier" ::: "memory")
; __device__ __forceinline__ void partialSM(f32x16& p0, f32x16& p1, float& m_reg, float& mn, float& alpha) {
;   constexpr float C = SCALE * 1.4426950408889634f;
;   float pmax = p0[0]; for (int r = 1; r < 16; ++r) pmax = fmaxf(pmax, p0[r]); for (int r = 0; r < 16; ++r) pmax = fmaxf(pmax, p1[r]);
;   { auto rr = __builtin_amdgcn_permlane32_swap(__float_as_uint(pmax), __float_as_uint(pmax), false, false);
;     pmax = fmaxf(__uint_as_float(rr[0]), __uint_as_float(rr[1])); }
;   if (__builtin_expect(__all(pmax - m_reg <= THR / SCALE), 1)) { mn = m_reg; alpha = 1.f; }
;   else { mn = fmaxf(m_reg, pmax); alpha = __builtin_amdgcn_exp2f((m_reg - mn) * C); m_reg = mn; }
;   float mnC = -mn * C;
;   for (int r = 0; r < 16; ++r) p0[r] = fmaf(p0[r], C, mnC); for (int r = 0; r < 16; ++r) p1[r] = fmaf(p1[r], C, mnC);
;   for (int r = 0; r < 16; ++r) p0[r] = __builtin_amdgcn_exp2f(p0[r]);
; }
; __device__ __forceinline__ void finishSM(f32x16& p0, f32x16& p1, float alpha, float& l_reg, bf16x8& pa0, bf16x8& pa1, bf16x8& pa2, bf16x8& pa3) {
;   for (int r = 0; r < 16; ++r) p1[r] = __builtin_amdgcn_exp2f(p1[r]);
;   float ps = 0; for (int r = 0; r < 16; ++r) ps += p0[r]; for (int r = 0; r < 16; ++r) ps += p1[r];
;   { auto rr = __builtin_amdgcn_permlane32_swap(__float_as_uint(ps), __float_as_uint(ps), false, false);
;     ps = __uint_as_float(rr[0]) + __uint_as_float(rr[1]); }
;   l_reg = l_reg * alpha + ps;
;     ...
;   PK4(p0, 0, pa0); PK4(p0, 8, pa1); PK4(p1, 0, pa2); PK4(p1, 8, pa3);
;     ...
; }
; __device__ __forceinline__ void attn_dma_body(const bf16_t* __restrict__ Qb, int ldq, int tpos0, const float* __restrict__ rope, const float* __restrict__ qgain, ...
;     ...
;   ATT_WAIT_BAR();
;   if (2 < NT) ATT_DMA(2, 2);
;   const int vb0 = (int)(uintptr_t)lds + 16384 + v_rd_base(lane);
;   f32x16 pA0, pA1, pB0, pB1; float mnA, mnB, alA, alB; bf16x8 pa0, pa1, pa2, pa3;
;   qkt(pA0, pA1, (const bf16_t*)lds, qr, r32, hi); partialSM(pA0, pA1, m_reg, mnA, alA);
.Lf16_noprio:
	s_waitcnt vmcnt(0) lgkmcnt(0)
	s_barrier
	s_add_u32 s2, s38, 0x8000
	s_addc_u32 s3, s39, 0
	s_add_u32 s4, s40, 0x8000
	s_addc_u32 s5, s41, 0
	s_add_i32 s6, s96, 0x10000
	s_mov_b32 m0, s6
	s_nop 0
	global_load_lds_dwordx4 v170, s[2:3]
	s_add_i32 m0, s6, 0x2000
	s_nop 0
	global_load_lds_dwordx4 v172, s[2:3]
	s_add_i32 m0, s6, 0x4000
	s_nop 0
	global_load_lds_dwordx4 v171, s[4:5]
	s_add_i32 m0, s6, 0x6000
	s_nop 0
	global_load_lds_dwordx4 v173, s[4:5]
	s_add_u32 s2, s2, 0x4000
	s_addc_u32 s3, s3, 0
	s_add_u32 s4, s4, 0x4000
	s_addc_u32 s5, s5, 0
	s_mov_b32 s36, 0
	v_add_u32_e32 v187, s36, v183
	v_add_u32_e32 v188, s36, v184
	v_add_u32_e32 v189, s36, v185
	v_add_u32_e32 v190, s36, v186
	ds_read_b128 v[146:149], v187 offset:0
	ds_read_b128 v[150:153], v187 offset:4096
	ds_read_b128 v[154:157], v187 offset:8192
	ds_read_b128 v[158:161], v187 offset:12288
	ds_read_b128 v[198:201], v188 offset:0
	ds_read_b128 v[202:205], v188 offset:4096
	ds_read_b128 v[206:209], v188 offset:8192
	ds_read_b128 v[210:213], v188 offset:12288
	s_waitcnt lgkmcnt(7)
	v_mfma_f32_16x16x32_bf16 v[66:69], v[146:149], v[98:101], 0
	v_mfma_f32_16x16x32_bf16 v[70:73], v[146:149], v[114:117], 0
	ds_read_b128 v[146:149], v189 offset:0
	s_waitcnt lgkmcnt(7)
	v_mfma_f32_16x16x32_bf16 v[74:77], v[150:153], v[98:101], 0
	v_mfma_f32_16x16x32_bf16 v[78:81], v[150:153], v[114:117], 0
	ds_read_b128 v[150:153], v189 offset:4096
	s_waitcnt lgkmcnt(7)
	v_mfma_f32_16x16x32_bf16 v[82:85], v[154:157], v[98:101], 0
	v_mfma_f32_16x16x32_bf16 v[86:89], v[154:157], v[114:117], 0
	ds_read_b128 v[154:157], v189 offset:8192
	s_waitcnt lgkmcnt(7)
	v_mfma_f32_16x16x32_bf16 v[90:93], v[158:161], v[98:101], 0
	v_mfma_f32_16x16x32_bf16 v[94:97], v[158:161], v[114:117], 0
	ds_read_b128 v[158:161], v189 offset:12288
	s_waitcnt lgkmcnt(7)
	v_mfma_f32_16x16x32_bf16 v[66:69], v[198:201], v[102:105], v[66:69]
	v_mfma_f32_16x16x32_bf16 v[70:73], v[198:201], v[118:121], v[70:73]
	ds_read_b128 v[198:201], v190 offset:0
	s_waitcnt lgkmcnt(7)
	v_mfma_f32_16x16x32_bf16 v[74:77], v[202:205], v[102:105], v[74:77]
	v_mfma_f32_16x16x32_bf16 v[78:81], v[202:205], v[118:121], v[78:81]
	ds_read_b128 v[202:205], v190 offset:4096
	s_waitcnt lgkmcnt(7)
	v_mfma_f32_16x16x32_bf16 v[82:85], v[206:209], v[102:105], v[82:85]
	v_mfma_f32_16x16x32_bf16 v[86:89], v[206:209], v[118:121], v[86:89]
	ds_read_b128 v[206:209], v190 offset:8192
	s_waitcnt lgkmcnt(7)
	v_mfma_f32_16x16x32_bf16 v[90:93], v[210:213], v[102:105], v[90:93]
	v_mfma_f32_16x16x32_bf16 v[94:97], v[210:213], v[118:121], v[94:97]
	ds_read_b128 v[210:213], v190 offset:12288
	s_waitcnt lgkmcnt(7)
	v_mfma_f32_16x16x32_bf16 v[66:69], v[146:149], v[106:109], v[66:69]
	v_mfma_f32_16x16x32_bf16 v[70:73], v[146:149], v[122:125], v[70:73]
	s_waitcnt lgkmcnt(6)
	v_mfma_f32_16x16x32_bf16 v[74:77], v[150:153], v[106:109], v[74:77]
	v_mfma_f32_16x16x32_bf16 v[78:81], v[150:153], v[122:125], v[78:81]
	s_waitcnt lgkmcnt(5)
	v_mfma_f32_16x16x32_bf16 v[82:85], v[154:157], v[106:109], v[82:85]
	v_mfma_f32_16x16x32_bf16 v[86:89], v[154:157], v[122:125], v[86:89]
	s_waitcnt lgkmcnt(4)
	v_mfma_f32_16x16x32_bf16 v[90:93], v[158:161], v[106:109], v[90:93]
	v_mfma_f32_16x16x32_bf16 v[94:97], v[158:161], v[122:125], v[94:97]
	s_waitcnt lgkmcnt(3)
	v_mfma_f32_16x16x32_bf16 v[66:69], v[198:201], v[110:113], v[66:69]
	v_mfma_f32_16x16x32_bf16 v[70:73], v[198:201], v[126:129], v[70:73]
	s_waitcnt lgkmcnt(2)
	v_mfma_f32_16x16x32_bf16 v[74:77], v[202:205], v[110:113], v[74:77]
	v_mfma_f32_16x16x32_bf16 v[78:81], v[202:205], v[126:129], v[78:81]
	s_waitcnt lgkmcnt(1)
	v_mfma_f32_16x16x32_bf16 v[82:85], v[206:209], v[110:113], v[82:85]
	v_mfma_f32_16x16x32_bf16 v[86:89], v[206:209], v[126:129], v[86:89]
	s_waitcnt lgkmcnt(0)
	v_mfma_f32_16x16x32_bf16 v[90:93], v[210:213], v[110:113], v[90:93]
	v_mfma_f32_16x16x32_bf16 v[94:97], v[210:213], v[126:129], v[94:97]
	s_nop 7
	v_exp_f32_e32 v66, v66
	v_exp_f32_e32 v67, v67
	v_exp_f32_e32 v68, v68
	v_exp_f32_e32 v69, v69
	v_exp_f32_e32 v70, v70
	v_exp_f32_e32 v71, v71
	v_exp_f32_e32 v72, v72
	v_exp_f32_e32 v73, v73
	v_exp_f32_e32 v74, v74
	v_exp_f32_e32 v75, v75
	v_exp_f32_e32 v76, v76
	v_exp_f32_e32 v77, v77
	v_exp_f32_e32 v78, v78
	v_exp_f32_e32 v79, v79
	v_exp_f32_e32 v80, v80
	v_exp_f32_e32 v81, v81
	v_exp_f32_e32 v82, v82
	v_exp_f32_e32 v83, v83
	v_exp_f32_e32 v84, v84
	v_exp_f32_e32 v85, v85
	v_exp_f32_e32 v86, v86
	v_exp_f32_e32 v87, v87
	v_exp_f32_e32 v88, v88
	v_exp_f32_e32 v89, v89
	v_exp_f32_e32 v90, v90
	v_exp_f32_e32 v91, v91
	v_exp_f32_e32 v92, v92
	v_exp_f32_e32 v93, v93
	v_exp_f32_e32 v94, v94
	v_exp_f32_e32 v95, v95
	v_exp_f32_e32 v96, v96
	v_exp_f32_e32 v97, v97
	v_add_f32_e32 v182, v182, v66
	v_add_f32_e32 v195, v195, v70
	v_add_f32_e32 v182, v182, v67
	v_add_f32_e32 v195, v195, v71
	v_add_f32_e32 v182, v182, v68
	v_add_f32_e32 v195, v195, v72
	v_add_f32_e32 v182, v182, v69
	v_add_f32_e32 v195, v195, v73
	v_add_f32_e32 v182, v182, v74
	v_add_f32_e32 v195, v195, v78
	v_add_f32_e32 v182, v182, v75
	v_add_f32_e32 v195, v195, v79
	v_add_f32_e32 v182, v182, v76
	v_add_f32_e32 v195, v195, v80
	v_add_f32_e32 v182, v182, v77
	v_add_f32_e32 v195, v195, v81
	v_add_f32_e32 v182, v182, v82
	v_add_f32_e32 v195, v195, v86
	v_add_f32_e32 v182, v182, v83
	v_add_f32_e32 v195, v195, v87
	v_add_f32_e32 v182, v182, v84
	v_add_f32_e32 v195, v195, v88
	v_add_f32_e32 v182, v182, v85
	v_add_f32_e32 v195, v195, v89
	v_add_f32_e32 v182, v182, v90
	v_add_f32_e32 v195, v195, v94
	v_add_f32_e32 v182, v182, v91
	v_add_f32_e32 v195, v195, v95
	v_add_f32_e32 v182, v182, v92
	v_add_f32_e32 v195, v195, v96
	v_add_f32_e32 v182, v182, v93
	v_add_f32_e32 v195, v195, v97
	v_cvt_pk_bf16_f32 v130, v66, v67
	v_cvt_pk_bf16_f32 v131, v68, v69
	v_cvt_pk_bf16_f32 v132, v74, v75
	v_cvt_pk_bf16_f32 v133, v76, v77
	v_cvt_pk_bf16_f32 v134, v82, v83
	v_cvt_pk_bf16_f32 v135, v84, v85
	v_cvt_pk_bf16_f32 v136, v90, v91
	v_cvt_pk_bf16_f32 v137, v92, v93
	v_cvt_pk_bf16_f32 v138, v70, v71
	v_cvt_pk_bf16_f32 v139, v72, v73
	v_cvt_pk_bf16_f32 v140, v78, v79
	v_cvt_pk_bf16_f32 v141, v80, v81
	v_cvt_pk_bf16_f32 v142, v86, v87
	v_cvt_pk_bf16_f32 v143, v88, v89
	v_cvt_pk_bf16_f32 v144, v94, v95
	v_cvt_pk_bf16_f32 v145, v96, v97
	s_mov_b32 s97, 1
	.p2align 6
